# GEMM loops: m0-hazard s_nop replaced by reordering the address add behind the m0 write (19 sites)
# baseline (speedup 1.0000x reference)
.LBB2_21:
	ds_read_b128 v[150:153], v145
	ds_read_b128 v[154:157], v145 offset:1024
	ds_read_b128 v[158:161], v145 offset:2048
	ds_read_b128 v[162:165], v145 offset:3072
	s_add_i32 s65, s28, 2
	s_add_u32 s30, s26, 0x80
	s_addc_u32 s29, s27, 0
	s_cmp_eq_u32 s55, s28
	s_cselect_b32 s28, s4, s30
	s_cselect_b32 s29, s5, s29
	s_cselect_b32 s31, s7, s64
	s_cselect_b32 s30, s6, s63
	v_lshl_add_u64 v[142:143], s[26:27], 0, v[136:137]
	s_add_i32 m0, s43, 0xc000
	ds_read_b128 v[166:169], v146
	ds_read_b128 v[170:173], v146 offset:1024
	ds_read_b128 v[174:177], v146 offset:2048
	ds_read_b128 v[178:181], v146 offset:3072
	ds_read_b128 v[182:185], v146 offset:4096
	ds_read_b128 v[186:189], v146 offset:5120
	ds_read_b128 v[190:193], v146 offset:6144
	ds_read_b128 v[194:197], v146 offset:7168
	global_load_lds_dwordx4 v[142:143], off
	s_add_i32 m0, s43, 0xe000
	v_lshl_add_u64 v[142:143], s[26:27], 0, v[134:135]
	global_load_lds_dwordx4 v[142:143], off
	s_waitcnt lgkmcnt(8)
	s_barrier
	s_waitcnt lgkmcnt(0)
	v_mfma_f32_16x16x32_f16 v[126:129], v[150:153], v[166:169], v[126:129]
	v_mfma_f32_16x16x32_f16 v[122:125], v[158:161], v[166:169], v[122:125]
	v_mfma_f32_16x16x32_f16 v[110:113], v[150:153], v[174:177], v[110:113]
	v_mfma_f32_16x16x32_f16 v[106:109], v[158:161], v[174:177], v[106:109]
	v_mfma_f32_16x16x32_f16 v[94:97], v[150:153], v[182:185], v[94:97]
	v_mfma_f32_16x16x32_f16 v[90:93], v[158:161], v[182:185], v[90:93]
	v_mfma_f32_16x16x32_f16 v[78:81], v[150:153], v[190:193], v[78:81]
	v_mfma_f32_16x16x32_f16 v[74:77], v[158:161], v[190:193], v[74:77]
	v_mfma_f32_16x16x32_f16 v[126:129], v[154:157], v[170:173], v[126:129]
	v_mfma_f32_16x16x32_f16 v[122:125], v[162:165], v[170:173], v[122:125]
	v_mfma_f32_16x16x32_f16 v[110:113], v[154:157], v[178:181], v[110:113]
	v_mfma_f32_16x16x32_f16 v[106:109], v[162:165], v[178:181], v[106:109]
	v_mfma_f32_16x16x32_f16 v[94:97], v[154:157], v[186:189], v[94:97]
	v_mfma_f32_16x16x32_f16 v[90:93], v[162:165], v[186:189], v[90:93]
	v_mfma_f32_16x16x32_f16 v[78:81], v[154:157], v[194:197], v[78:81]
	v_mfma_f32_16x16x32_f16 v[74:77], v[162:165], v[194:197], v[74:77]
	s_barrier
	s_add_i32 s66, s57, s40
	v_lshl_add_u64 v[142:143], s[30:31], 0, v[130:131]
	s_mov_b32 m0, s66
	ds_read_b128 v[198:201], v147
	ds_read_b128 v[202:205], v147 offset:1024
	ds_read_b128 v[206:209], v147 offset:2048
	ds_read_b128 v[210:213], v147 offset:3072
	global_load_lds_dwordx4 v[142:143], off
	s_add_i32 m0, s66, 0x2000
	v_lshl_add_u64 v[214:215], s[30:31], 0, v[132:133]
	global_load_lds_dwordx4 v[214:215], off
	s_barrier
	s_waitcnt lgkmcnt(0)
	v_mfma_f32_16x16x32_f16 v[118:121], v[198:201], v[166:169], v[118:121]
	v_mfma_f32_16x16x32_f16 v[114:117], v[206:209], v[166:169], v[114:117]
	v_mfma_f32_16x16x32_f16 v[102:105], v[198:201], v[174:177], v[102:105]
	v_mfma_f32_16x16x32_f16 v[98:101], v[206:209], v[174:177], v[98:101]
	v_mfma_f32_16x16x32_f16 v[86:89], v[198:201], v[182:185], v[86:89]
	v_mfma_f32_16x16x32_f16 v[82:85], v[206:209], v[182:185], v[82:85]
	v_mfma_f32_16x16x32_f16 v[70:73], v[198:201], v[190:193], v[70:73]
	v_mfma_f32_16x16x32_f16 v[66:69], v[206:209], v[190:193], v[66:69]
	v_mfma_f32_16x16x32_f16 v[118:121], v[202:205], v[170:173], v[118:121]
	v_mfma_f32_16x16x32_f16 v[114:117], v[210:213], v[170:173], v[114:117]
	v_mfma_f32_16x16x32_f16 v[102:105], v[202:205], v[178:181], v[102:105]
	v_mfma_f32_16x16x32_f16 v[98:101], v[210:213], v[178:181], v[98:101]
	v_mfma_f32_16x16x32_f16 v[86:89], v[202:205], v[186:189], v[86:89]
	v_mfma_f32_16x16x32_f16 v[82:85], v[210:213], v[186:189], v[82:85]
	v_mfma_f32_16x16x32_f16 v[70:73], v[202:205], v[194:197], v[70:73]
	v_mfma_f32_16x16x32_f16 v[66:69], v[210:213], v[194:197], v[66:69]
	s_mov_b32 m0, s43
	v_lshl_add_u64 v[216:217], s[28:29], 0, v[130:131]
	s_barrier
	ds_read_b128 v[166:169], v146 offset:16384
	ds_read_b128 v[170:173], v146 offset:17408
	ds_read_b128 v[174:177], v146 offset:18432
	ds_read_b128 v[178:181], v146 offset:19456
	ds_read_b128 v[182:185], v146 offset:20480
	ds_read_b128 v[186:189], v146 offset:21504
	ds_read_b128 v[190:193], v146 offset:22528
	ds_read_b128 v[194:197], v146 offset:23552
	global_load_lds_dwordx4 v[216:217], off
	s_mov_b32 m0, s44
	v_lshl_add_u64 v[218:219], s[28:29], 0, v[132:133]
	global_load_lds_dwordx4 v[218:219], off
	s_barrier
	s_waitcnt lgkmcnt(0)
	v_mfma_f32_16x16x32_f16 v[62:65], v[150:153], v[166:169], v[62:65]
	v_mfma_f32_16x16x32_f16 v[58:61], v[158:161], v[166:169], v[58:61]
	v_mfma_f32_16x16x32_f16 v[46:49], v[150:153], v[174:177], v[46:49]
	v_mfma_f32_16x16x32_f16 v[42:45], v[158:161], v[174:177], v[42:45]
	v_mfma_f32_16x16x32_f16 v[30:33], v[150:153], v[182:185], v[30:33]
	v_mfma_f32_16x16x32_f16 v[26:29], v[158:161], v[182:185], v[26:29]
	v_mfma_f32_16x16x32_f16 v[14:17], v[150:153], v[190:193], v[14:17]
	v_mfma_f32_16x16x32_f16 v[10:13], v[158:161], v[190:193], v[10:13]
	v_mfma_f32_16x16x32_f16 v[62:65], v[154:157], v[170:173], v[62:65]
	v_mfma_f32_16x16x32_f16 v[58:61], v[162:165], v[170:173], v[58:61]
	v_mfma_f32_16x16x32_f16 v[46:49], v[154:157], v[178:181], v[46:49]
	v_mfma_f32_16x16x32_f16 v[42:45], v[162:165], v[178:181], v[42:45]
	v_mfma_f32_16x16x32_f16 v[30:33], v[154:157], v[186:189], v[30:33]
	v_mfma_f32_16x16x32_f16 v[26:29], v[162:165], v[186:189], v[26:29]
	v_mfma_f32_16x16x32_f16 v[14:17], v[154:157], v[194:197], v[14:17]
	v_mfma_f32_16x16x32_f16 v[10:13], v[162:165], v[194:197], v[10:13]
	s_barrier
	s_add_u32 s30, s30, s10
	s_addc_u32 s31, s31, s11
	s_add_i32 s66, s58, s40
	v_lshl_add_u64 v[220:221], s[30:31], 0, v[130:131]
	s_mov_b32 m0, s66
	v_lshl_add_u64 v[222:223], s[30:31], 0, v[132:133]
	global_load_lds_dwordx4 v[220:221], off
	s_add_i32 m0, s66, 0x2000
	s_nop 0
	global_load_lds_dwordx4 v[222:223], off
	s_waitcnt vmcnt(6)
	s_barrier
	v_mfma_f32_16x16x32_f16 v[54:57], v[198:201], v[166:169], v[54:57]
	v_mfma_f32_16x16x32_f16 v[50:53], v[206:209], v[166:169], v[50:53]
	v_mfma_f32_16x16x32_f16 v[38:41], v[198:201], v[174:177], v[38:41]
	v_mfma_f32_16x16x32_f16 v[34:37], v[206:209], v[174:177], v[34:37]
	v_mfma_f32_16x16x32_f16 v[22:25], v[198:201], v[182:185], v[22:25]
	v_mfma_f32_16x16x32_f16 v[18:21], v[206:209], v[182:185], v[18:21]
	v_mfma_f32_16x16x32_f16 v[6:9], v[198:201], v[190:193], v[6:9]
	v_mfma_f32_16x16x32_f16 v[2:5], v[206:209], v[190:193], v[2:5]
	v_mfma_f32_16x16x32_f16 v[54:57], v[202:205], v[170:173], v[54:57]
	v_mfma_f32_16x16x32_f16 v[50:53], v[210:213], v[170:173], v[50:53]
	v_mfma_f32_16x16x32_f16 v[38:41], v[202:205], v[178:181], v[38:41]
	v_mfma_f32_16x16x32_f16 v[34:37], v[210:213], v[178:181], v[34:37]
	v_mfma_f32_16x16x32_f16 v[22:25], v[202:205], v[186:189], v[22:25]
	v_mfma_f32_16x16x32_f16 v[18:21], v[210:213], v[186:189], v[18:21]
	v_mfma_f32_16x16x32_f16 v[6:9], v[202:205], v[194:197], v[6:9]
	v_mfma_f32_16x16x32_f16 v[2:5], v[210:213], v[194:197], v[2:5]
	s_add_i32 s30, 0, 0x18000
	v_add_u32_e32 v140, s30, v141
	s_barrier
	ds_read_b128 v[150:153], v140
	ds_read_b128 v[154:157], v140 offset:1024
	ds_read_b128 v[158:161], v140 offset:2048
	ds_read_b128 v[162:165], v140 offset:3072
	s_add_u32 s28, s28, s10
	s_addc_u32 s29, s29, s11
	s_mov_b32 m0, s45
	v_lshl_add_u64 v[198:199], s[28:29], 0, v[130:131]
	ds_read_b128 v[166:169], v146 offset:32768
	ds_read_b128 v[170:173], v146 offset:33792
	ds_read_b128 v[174:177], v146 offset:34816
	ds_read_b128 v[178:181], v146 offset:35840
	ds_read_b128 v[182:185], v146 offset:36864
	ds_read_b128 v[186:189], v146 offset:37888
	ds_read_b128 v[190:193], v146 offset:38912
	ds_read_b128 v[194:197], v146 offset:39936
	global_load_lds_dwordx4 v[198:199], off
	s_mov_b32 m0, s46
	v_lshl_add_u64 v[198:199], s[28:29], 0, v[132:133]
	global_load_lds_dwordx4 v[198:199], off
	s_waitcnt lgkmcnt(8)
	s_barrier
	s_waitcnt lgkmcnt(0)
	v_mfma_f32_16x16x32_f16 v[126:129], v[150:153], v[166:169], v[126:129]
	v_mfma_f32_16x16x32_f16 v[122:125], v[158:161], v[166:169], v[122:125]
	v_mfma_f32_16x16x32_f16 v[110:113], v[150:153], v[174:177], v[110:113]
	v_mfma_f32_16x16x32_f16 v[106:109], v[158:161], v[174:177], v[106:109]
	v_mfma_f32_16x16x32_f16 v[94:97], v[150:153], v[182:185], v[94:97]
	v_mfma_f32_16x16x32_f16 v[90:93], v[158:161], v[182:185], v[90:93]
	v_mfma_f32_16x16x32_f16 v[78:81], v[150:153], v[190:193], v[78:81]
	v_mfma_f32_16x16x32_f16 v[74:77], v[158:161], v[190:193], v[74:77]
	v_mfma_f32_16x16x32_f16 v[126:129], v[154:157], v[170:173], v[126:129]
	v_mfma_f32_16x16x32_f16 v[122:125], v[162:165], v[170:173], v[122:125]
	v_mfma_f32_16x16x32_f16 v[110:113], v[154:157], v[178:181], v[110:113]
	v_mfma_f32_16x16x32_f16 v[106:109], v[162:165], v[178:181], v[106:109]
	v_mfma_f32_16x16x32_f16 v[94:97], v[154:157], v[186:189], v[94:97]
	v_mfma_f32_16x16x32_f16 v[90:93], v[162:165], v[186:189], v[90:93]
	v_mfma_f32_16x16x32_f16 v[78:81], v[154:157], v[194:197], v[78:81]
	v_mfma_f32_16x16x32_f16 v[74:77], v[162:165], v[194:197], v[74:77]
	s_barrier
	s_add_i32 s28, 0, 0x1c000
	s_add_i32 s29, s30, s40
	v_add_u32_e32 v140, s28, v141
	v_lshl_add_u64 v[142:143], v[142:143], 0, s[22:23]
	s_mov_b32 m0, s29
	ds_read_b128 v[198:201], v140
	ds_read_b128 v[202:205], v140 offset:1024
	ds_read_b128 v[206:209], v140 offset:2048
	ds_read_b128 v[210:213], v140 offset:3072
	global_load_lds_dwordx4 v[142:143], off
	s_add_i32 m0, s29, 0x2000
	v_lshl_add_u64 v[142:143], v[214:215], 0, s[22:23]
	global_load_lds_dwordx4 v[142:143], off
	s_barrier
	s_waitcnt lgkmcnt(0)
	v_mfma_f32_16x16x32_f16 v[118:121], v[198:201], v[166:169], v[118:121]
	v_mfma_f32_16x16x32_f16 v[114:117], v[206:209], v[166:169], v[114:117]
	v_mfma_f32_16x16x32_f16 v[102:105], v[198:201], v[174:177], v[102:105]
	v_mfma_f32_16x16x32_f16 v[98:101], v[206:209], v[174:177], v[98:101]
	v_mfma_f32_16x16x32_f16 v[86:89], v[198:201], v[182:185], v[86:89]
	v_mfma_f32_16x16x32_f16 v[82:85], v[206:209], v[182:185], v[82:85]
	v_mfma_f32_16x16x32_f16 v[70:73], v[198:201], v[190:193], v[70:73]
	v_mfma_f32_16x16x32_f16 v[66:69], v[206:209], v[190:193], v[66:69]
	v_mfma_f32_16x16x32_f16 v[118:121], v[202:205], v[170:173], v[118:121]
	v_mfma_f32_16x16x32_f16 v[114:117], v[210:213], v[170:173], v[114:117]
	v_mfma_f32_16x16x32_f16 v[102:105], v[202:205], v[178:181], v[102:105]
	v_mfma_f32_16x16x32_f16 v[98:101], v[210:213], v[178:181], v[98:101]
	v_mfma_f32_16x16x32_f16 v[86:89], v[202:205], v[186:189], v[86:89]
	v_mfma_f32_16x16x32_f16 v[82:85], v[210:213], v[186:189], v[82:85]
	v_mfma_f32_16x16x32_f16 v[70:73], v[202:205], v[194:197], v[70:73]
	v_mfma_f32_16x16x32_f16 v[66:69], v[210:213], v[194:197], v[66:69]
	s_mov_b32 m0, s49
	v_lshl_add_u64 v[142:143], v[216:217], 0, s[22:23]
	s_barrier
	ds_read_b128 v[166:169], v146 offset:49152
	ds_read_b128 v[170:173], v146 offset:50176
	ds_read_b128 v[174:177], v146 offset:51200
	ds_read_b128 v[178:181], v146 offset:52224
	ds_read_b128 v[182:185], v146 offset:53248
	ds_read_b128 v[186:189], v146 offset:54272
	ds_read_b128 v[190:193], v146 offset:55296
	ds_read_b128 v[194:197], v146 offset:56320
	global_load_lds_dwordx4 v[142:143], off
	s_mov_b32 m0, s50
	v_lshl_add_u64 v[142:143], v[218:219], 0, s[22:23]
	global_load_lds_dwordx4 v[142:143], off
	s_barrier
	s_waitcnt lgkmcnt(0)
	v_mfma_f32_16x16x32_f16 v[62:65], v[150:153], v[166:169], v[62:65]
	v_mfma_f32_16x16x32_f16 v[58:61], v[158:161], v[166:169], v[58:61]
	v_mfma_f32_16x16x32_f16 v[46:49], v[150:153], v[174:177], v[46:49]
	v_mfma_f32_16x16x32_f16 v[42:45], v[158:161], v[174:177], v[42:45]
	v_mfma_f32_16x16x32_f16 v[30:33], v[150:153], v[182:185], v[30:33]
	v_mfma_f32_16x16x32_f16 v[26:29], v[158:161], v[182:185], v[26:29]
	v_mfma_f32_16x16x32_f16 v[14:17], v[150:153], v[190:193], v[14:17]
	v_mfma_f32_16x16x32_f16 v[10:13], v[158:161], v[190:193], v[10:13]
	v_mfma_f32_16x16x32_f16 v[62:65], v[154:157], v[170:173], v[62:65]
	v_mfma_f32_16x16x32_f16 v[58:61], v[162:165], v[170:173], v[58:61]
	v_mfma_f32_16x16x32_f16 v[46:49], v[154:157], v[178:181], v[46:49]
	v_mfma_f32_16x16x32_f16 v[42:45], v[162:165], v[178:181], v[42:45]
	v_mfma_f32_16x16x32_f16 v[30:33], v[154:157], v[186:189], v[30:33]
	v_mfma_f32_16x16x32_f16 v[26:29], v[162:165], v[186:189], v[26:29]
	v_mfma_f32_16x16x32_f16 v[14:17], v[154:157], v[194:197], v[14:17]
	v_mfma_f32_16x16x32_f16 v[10:13], v[162:165], v[194:197], v[10:13]
	s_barrier
	s_add_i32 s28, s28, s40
	s_mov_b32 m0, s28
	v_lshl_add_u64 v[142:143], v[220:221], 0, s[22:23]
	global_load_lds_dwordx4 v[142:143], off
	s_add_i32 m0, s28, 0x2000
	v_lshl_add_u64 v[142:143], v[222:223], 0, s[22:23]
	global_load_lds_dwordx4 v[142:143], off
	s_waitcnt vmcnt(6)
	s_barrier
	v_mfma_f32_16x16x32_f16 v[54:57], v[198:201], v[166:169], v[54:57]
	v_mfma_f32_16x16x32_f16 v[50:53], v[206:209], v[166:169], v[50:53]
	v_mfma_f32_16x16x32_f16 v[38:41], v[198:201], v[174:177], v[38:41]
	v_mfma_f32_16x16x32_f16 v[34:37], v[206:209], v[174:177], v[34:37]
	v_mfma_f32_16x16x32_f16 v[22:25], v[198:201], v[182:185], v[22:25]
	v_mfma_f32_16x16x32_f16 v[18:21], v[206:209], v[182:185], v[18:21]
	v_mfma_f32_16x16x32_f16 v[6:9], v[198:201], v[190:193], v[6:9]
	v_mfma_f32_16x16x32_f16 v[2:5], v[206:209], v[190:193], v[2:5]
	v_mfma_f32_16x16x32_f16 v[54:57], v[202:205], v[170:173], v[54:57]
	v_mfma_f32_16x16x32_f16 v[50:53], v[210:213], v[170:173], v[50:53]
	v_mfma_f32_16x16x32_f16 v[38:41], v[202:205], v[178:181], v[38:41]
	v_mfma_f32_16x16x32_f16 v[34:37], v[210:213], v[178:181], v[34:37]
	v_mfma_f32_16x16x32_f16 v[22:25], v[202:205], v[186:189], v[22:25]
	v_mfma_f32_16x16x32_f16 v[18:21], v[210:213], v[186:189], v[18:21]
	v_mfma_f32_16x16x32_f16 v[6:9], v[202:205], v[194:197], v[6:9]
	v_mfma_f32_16x16x32_f16 v[2:5], v[210:213], v[194:197], v[2:5]
	s_add_u32 s63, s63, 0x100
	s_addc_u32 s64, s64, 0
	s_add_u32 s26, s26, 0x100
	s_addc_u32 s27, s27, 0
	s_cmp_ge_i32 s65, s51
	s_mov_b32 s28, s65
	s_barrier
	s_cbranch_scc0 .LBB2_21
	s_branch .LBB2_8

.LBB3_23:
	ds_read_b128 v[128:131], v169
	ds_read_b128 v[132:135], v169 offset:1024
	ds_read_b128 v[136:139], v169 offset:2048
	ds_read_b128 v[140:143], v169 offset:3072
	s_add_i32 s71, s34, 2
	s_add_u32 s36, s30, 0x80
	s_addc_u32 s35, s31, 0
	s_cmp_eq_u32 s62, s34
	s_cselect_b32 s34, s28, s36
	s_cselect_b32 s35, s29, s35
	s_cselect_b32 s37, s5, s70
	s_cselect_b32 s36, s4, s69
	v_lshl_add_u64 v[200:201], s[30:31], 0, v[150:151]
	s_add_i32 m0, s51, 0xc000
	ds_read_b128 v[154:157], v170
	ds_read_b128 v[172:175], v170 offset:1024
	ds_read_b128 v[176:179], v170 offset:2048
	ds_read_b128 v[180:183], v170 offset:3072
	ds_read_b128 v[184:187], v170 offset:4096
	ds_read_b128 v[188:191], v170 offset:5120
	ds_read_b128 v[192:195], v170 offset:6144
	ds_read_b128 v[196:199], v170 offset:7168
	global_load_lds_dwordx4 v[200:201], off
	s_add_i32 m0, s51, 0xe000
	v_lshl_add_u64 v[200:201], s[30:31], 0, v[148:149]
	global_load_lds_dwordx4 v[200:201], off
	s_waitcnt lgkmcnt(8)
	s_barrier
	s_waitcnt lgkmcnt(0)
	v_mfma_f32_16x16x32_f16 v[116:119], v[128:131], v[154:157], v[116:119]
	v_mfma_f32_16x16x32_f16 v[124:127], v[136:139], v[154:157], v[124:127]
	v_mfma_f32_16x16x32_f16 v[108:111], v[128:131], v[176:179], v[108:111]
	v_mfma_f32_16x16x32_f16 v[104:107], v[136:139], v[176:179], v[104:107]
	v_mfma_f32_16x16x32_f16 v[92:95], v[128:131], v[184:187], v[92:95]
	v_mfma_f32_16x16x32_f16 v[88:91], v[136:139], v[184:187], v[88:91]
	v_mfma_f32_16x16x32_f16 v[76:79], v[128:131], v[192:195], v[76:79]
	v_mfma_f32_16x16x32_f16 v[72:75], v[136:139], v[192:195], v[72:75]
	v_mfma_f32_16x16x32_f16 v[116:119], v[132:135], v[172:175], v[116:119]
	v_mfma_f32_16x16x32_f16 v[124:127], v[140:143], v[172:175], v[124:127]
	v_mfma_f32_16x16x32_f16 v[108:111], v[132:135], v[180:183], v[108:111]
	v_mfma_f32_16x16x32_f16 v[104:107], v[140:143], v[180:183], v[104:107]
	v_mfma_f32_16x16x32_f16 v[92:95], v[132:135], v[188:191], v[92:95]
	v_mfma_f32_16x16x32_f16 v[88:91], v[140:143], v[188:191], v[88:91]
	v_mfma_f32_16x16x32_f16 v[76:79], v[132:135], v[196:199], v[76:79]
	v_mfma_f32_16x16x32_f16 v[72:75], v[140:143], v[196:199], v[72:75]
	s_barrier
	s_add_i32 s72, s63, s40
	v_lshl_add_u64 v[216:217], s[36:37], 0, v[144:145]
	s_mov_b32 m0, s72
	ds_read_b128 v[200:203], v171
	ds_read_b128 v[204:207], v171 offset:1024
	ds_read_b128 v[208:211], v171 offset:2048
	ds_read_b128 v[212:215], v171 offset:3072
	global_load_lds_dwordx4 v[216:217], off
	s_add_i32 m0, s72, 0x2000
	v_lshl_add_u64 v[218:219], s[36:37], 0, v[146:147]
	global_load_lds_dwordx4 v[218:219], off
	s_barrier
	s_waitcnt lgkmcnt(0)
	v_mfma_f32_16x16x32_f16 v[120:123], v[200:203], v[154:157], v[120:123]
	v_mfma_f32_16x16x32_f16 v[112:115], v[208:211], v[154:157], v[112:115]
	v_mfma_f32_16x16x32_f16 v[100:103], v[200:203], v[176:179], v[100:103]
	v_mfma_f32_16x16x32_f16 v[96:99], v[208:211], v[176:179], v[96:99]
	v_mfma_f32_16x16x32_f16 v[84:87], v[200:203], v[184:187], v[84:87]
	v_mfma_f32_16x16x32_f16 v[80:83], v[208:211], v[184:187], v[80:83]
	v_mfma_f32_16x16x32_f16 v[68:71], v[200:203], v[192:195], v[68:71]
	v_mfma_f32_16x16x32_f16 v[64:67], v[208:211], v[192:195], v[64:67]
	v_mfma_f32_16x16x32_f16 v[120:123], v[204:207], v[172:175], v[120:123]
	v_mfma_f32_16x16x32_f16 v[112:115], v[212:215], v[172:175], v[112:115]
	v_mfma_f32_16x16x32_f16 v[100:103], v[204:207], v[180:183], v[100:103]
	v_mfma_f32_16x16x32_f16 v[96:99], v[212:215], v[180:183], v[96:99]
	v_mfma_f32_16x16x32_f16 v[84:87], v[204:207], v[188:191], v[84:87]
	v_mfma_f32_16x16x32_f16 v[80:83], v[212:215], v[188:191], v[80:83]
	v_mfma_f32_16x16x32_f16 v[68:71], v[204:207], v[196:199], v[68:71]
	v_mfma_f32_16x16x32_f16 v[64:67], v[212:215], v[196:199], v[64:67]
	s_mov_b32 m0, s51
	v_lshl_add_u64 v[220:221], s[34:35], 0, v[144:145]
	s_barrier
	ds_read_b128 v[154:157], v170 offset:16384
	ds_read_b128 v[172:175], v170 offset:17408
	ds_read_b128 v[176:179], v170 offset:18432
	ds_read_b128 v[180:183], v170 offset:19456
	ds_read_b128 v[184:187], v170 offset:20480
	ds_read_b128 v[188:191], v170 offset:21504
	ds_read_b128 v[192:195], v170 offset:22528
	ds_read_b128 v[196:199], v170 offset:23552
	global_load_lds_dwordx4 v[220:221], off
	s_mov_b32 m0, s52
	v_lshl_add_u64 v[222:223], s[34:35], 0, v[146:147]
	global_load_lds_dwordx4 v[222:223], off
	s_barrier
	s_waitcnt lgkmcnt(0)
	v_mfma_f32_16x16x32_f16 v[60:63], v[128:131], v[154:157], v[60:63]
	v_mfma_f32_16x16x32_f16 v[56:59], v[136:139], v[154:157], v[56:59]
	v_mfma_f32_16x16x32_f16 v[44:47], v[128:131], v[176:179], v[44:47]
	v_mfma_f32_16x16x32_f16 v[40:43], v[136:139], v[176:179], v[40:43]
	v_mfma_f32_16x16x32_f16 v[28:31], v[128:131], v[184:187], v[28:31]
	v_mfma_f32_16x16x32_f16 v[24:27], v[136:139], v[184:187], v[24:27]
	v_mfma_f32_16x16x32_f16 v[12:15], v[128:131], v[192:195], v[12:15]
	v_mfma_f32_16x16x32_f16 v[8:11], v[136:139], v[192:195], v[8:11]
	v_mfma_f32_16x16x32_f16 v[60:63], v[132:135], v[172:175], v[60:63]
	v_mfma_f32_16x16x32_f16 v[56:59], v[140:143], v[172:175], v[56:59]
	v_mfma_f32_16x16x32_f16 v[44:47], v[132:135], v[180:183], v[44:47]
	v_mfma_f32_16x16x32_f16 v[40:43], v[140:143], v[180:183], v[40:43]
	v_mfma_f32_16x16x32_f16 v[28:31], v[132:135], v[188:191], v[28:31]
	v_mfma_f32_16x16x32_f16 v[24:27], v[140:143], v[188:191], v[24:27]
	v_mfma_f32_16x16x32_f16 v[12:15], v[132:135], v[196:199], v[12:15]
	v_mfma_f32_16x16x32_f16 v[8:11], v[140:143], v[196:199], v[8:11]
	s_barrier
	s_add_u32 s36, s36, s20
	s_addc_u32 s37, s37, s21
	s_add_i32 s72, s64, s40
	v_lshl_add_u64 v[224:225], s[36:37], 0, v[144:145]
	s_mov_b32 m0, s72
	v_lshl_add_u64 v[226:227], s[36:37], 0, v[146:147]
	global_load_lds_dwordx4 v[224:225], off
	s_add_i32 m0, s72, 0x2000
	s_nop 0
	global_load_lds_dwordx4 v[226:227], off
	s_waitcnt vmcnt(6)
	s_barrier
	v_mfma_f32_16x16x32_f16 v[52:55], v[200:203], v[154:157], v[52:55]
	v_mfma_f32_16x16x32_f16 v[48:51], v[208:211], v[154:157], v[48:51]
	v_mfma_f32_16x16x32_f16 v[36:39], v[200:203], v[176:179], v[36:39]
	v_mfma_f32_16x16x32_f16 v[32:35], v[208:211], v[176:179], v[32:35]
	v_mfma_f32_16x16x32_f16 v[20:23], v[200:203], v[184:187], v[20:23]
	v_mfma_f32_16x16x32_f16 v[16:19], v[208:211], v[184:187], v[16:19]
	v_mfma_f32_16x16x32_f16 v[4:7], v[200:203], v[192:195], v[4:7]
	v_mfma_f32_16x16x32_f16 v[0:3], v[208:211], v[192:195], v[0:3]
	v_mfma_f32_16x16x32_f16 v[52:55], v[204:207], v[172:175], v[52:55]
	v_mfma_f32_16x16x32_f16 v[48:51], v[212:215], v[172:175], v[48:51]
	v_mfma_f32_16x16x32_f16 v[36:39], v[204:207], v[180:183], v[36:39]
	v_mfma_f32_16x16x32_f16 v[32:35], v[212:215], v[180:183], v[32:35]
	v_mfma_f32_16x16x32_f16 v[20:23], v[204:207], v[188:191], v[20:23]
	v_mfma_f32_16x16x32_f16 v[16:19], v[212:215], v[188:191], v[16:19]
	v_mfma_f32_16x16x32_f16 v[4:7], v[204:207], v[196:199], v[4:7]
	v_mfma_f32_16x16x32_f16 v[0:3], v[212:215], v[196:199], v[0:3]
	s_add_i32 s36, 0, 0x18000
	v_add_u32_e32 v140, s36, v161
	s_barrier
	ds_read_b128 v[128:131], v140
	ds_read_b128 v[132:135], v140 offset:1024
	ds_read_b128 v[136:139], v140 offset:2048
	ds_read_b128 v[140:143], v140 offset:3072
	s_add_u32 s34, s34, s20
	s_addc_u32 s35, s35, s21
	s_mov_b32 m0, s53
	v_lshl_add_u64 v[200:201], s[34:35], 0, v[144:145]
	ds_read_b128 v[154:157], v170 offset:32768
	ds_read_b128 v[172:175], v170 offset:33792
	ds_read_b128 v[176:179], v170 offset:34816
	ds_read_b128 v[180:183], v170 offset:35840
	ds_read_b128 v[184:187], v170 offset:36864
	ds_read_b128 v[188:191], v170 offset:37888
	ds_read_b128 v[192:195], v170 offset:38912
	ds_read_b128 v[196:199], v170 offset:39936
	global_load_lds_dwordx4 v[200:201], off
	s_mov_b32 m0, s54
	v_lshl_add_u64 v[200:201], s[34:35], 0, v[146:147]
	global_load_lds_dwordx4 v[200:201], off
	s_waitcnt lgkmcnt(8)
	s_barrier
	s_waitcnt lgkmcnt(0)
	v_mfma_f32_16x16x32_f16 v[116:119], v[128:131], v[154:157], v[116:119]
	v_mfma_f32_16x16x32_f16 v[124:127], v[136:139], v[154:157], v[124:127]
	v_mfma_f32_16x16x32_f16 v[108:111], v[128:131], v[176:179], v[108:111]
	v_mfma_f32_16x16x32_f16 v[104:107], v[136:139], v[176:179], v[104:107]
	v_mfma_f32_16x16x32_f16 v[92:95], v[128:131], v[184:187], v[92:95]
	v_mfma_f32_16x16x32_f16 v[88:91], v[136:139], v[184:187], v[88:91]
	v_mfma_f32_16x16x32_f16 v[76:79], v[128:131], v[192:195], v[76:79]
	v_mfma_f32_16x16x32_f16 v[72:75], v[136:139], v[192:195], v[72:75]
	v_mfma_f32_16x16x32_f16 v[116:119], v[132:135], v[172:175], v[116:119]
	v_mfma_f32_16x16x32_f16 v[124:127], v[140:143], v[172:175], v[124:127]
	v_mfma_f32_16x16x32_f16 v[108:111], v[132:135], v[180:183], v[108:111]
	v_mfma_f32_16x16x32_f16 v[104:107], v[140:143], v[180:183], v[104:107]
	v_mfma_f32_16x16x32_f16 v[92:95], v[132:135], v[188:191], v[92:95]
	v_mfma_f32_16x16x32_f16 v[88:91], v[140:143], v[188:191], v[88:91]
	v_mfma_f32_16x16x32_f16 v[76:79], v[132:135], v[196:199], v[76:79]
	v_mfma_f32_16x16x32_f16 v[72:75], v[140:143], v[196:199], v[72:75]
	s_barrier
	s_add_i32 s34, 0, 0x1c000
	s_add_i32 s35, s36, s40
	v_add_u32_e32 v212, s34, v161
	v_lshl_add_u64 v[216:217], v[216:217], 0, s[24:25]
	s_mov_b32 m0, s35
	ds_read_b128 v[200:203], v212
	ds_read_b128 v[204:207], v212 offset:1024
	ds_read_b128 v[208:211], v212 offset:2048
	ds_read_b128 v[212:215], v212 offset:3072
	global_load_lds_dwordx4 v[216:217], off
	s_add_i32 m0, s35, 0x2000
	v_lshl_add_u64 v[216:217], v[218:219], 0, s[24:25]
	global_load_lds_dwordx4 v[216:217], off
	s_barrier
	s_waitcnt lgkmcnt(0)
	v_mfma_f32_16x16x32_f16 v[120:123], v[200:203], v[154:157], v[120:123]
	v_mfma_f32_16x16x32_f16 v[112:115], v[208:211], v[154:157], v[112:115]
	v_mfma_f32_16x16x32_f16 v[100:103], v[200:203], v[176:179], v[100:103]
	v_mfma_f32_16x16x32_f16 v[96:99], v[208:211], v[176:179], v[96:99]
	v_mfma_f32_16x16x32_f16 v[84:87], v[200:203], v[184:187], v[84:87]
	v_mfma_f32_16x16x32_f16 v[80:83], v[208:211], v[184:187], v[80:83]
	v_mfma_f32_16x16x32_f16 v[68:71], v[200:203], v[192:195], v[68:71]
	v_mfma_f32_16x16x32_f16 v[64:67], v[208:211], v[192:195], v[64:67]
	v_mfma_f32_16x16x32_f16 v[120:123], v[204:207], v[172:175], v[120:123]
	v_mfma_f32_16x16x32_f16 v[112:115], v[212:215], v[172:175], v[112:115]
	v_mfma_f32_16x16x32_f16 v[100:103], v[204:207], v[180:183], v[100:103]
	v_mfma_f32_16x16x32_f16 v[96:99], v[212:215], v[180:183], v[96:99]
	v_mfma_f32_16x16x32_f16 v[84:87], v[204:207], v[188:191], v[84:87]
	v_mfma_f32_16x16x32_f16 v[80:83], v[212:215], v[188:191], v[80:83]
	v_mfma_f32_16x16x32_f16 v[68:71], v[204:207], v[196:199], v[68:71]
	v_mfma_f32_16x16x32_f16 v[64:67], v[212:215], v[196:199], v[64:67]
	s_mov_b32 m0, s57
	v_lshl_add_u64 v[216:217], v[220:221], 0, s[24:25]
	s_barrier
	ds_read_b128 v[154:157], v170 offset:49152
	ds_read_b128 v[172:175], v170 offset:50176
	ds_read_b128 v[176:179], v170 offset:51200
	ds_read_b128 v[180:183], v170 offset:52224
	ds_read_b128 v[184:187], v170 offset:53248
	ds_read_b128 v[188:191], v170 offset:54272
	ds_read_b128 v[192:195], v170 offset:55296
	ds_read_b128 v[196:199], v170 offset:56320
	global_load_lds_dwordx4 v[216:217], off
	s_mov_b32 m0, s58
	v_lshl_add_u64 v[216:217], v[222:223], 0, s[24:25]
	global_load_lds_dwordx4 v[216:217], off
	s_barrier
	s_waitcnt lgkmcnt(0)
	v_mfma_f32_16x16x32_f16 v[60:63], v[128:131], v[154:157], v[60:63]
	v_mfma_f32_16x16x32_f16 v[56:59], v[136:139], v[154:157], v[56:59]
	v_mfma_f32_16x16x32_f16 v[44:47], v[128:131], v[176:179], v[44:47]
	v_mfma_f32_16x16x32_f16 v[40:43], v[136:139], v[176:179], v[40:43]
	v_mfma_f32_16x16x32_f16 v[28:31], v[128:131], v[184:187], v[28:31]
	v_mfma_f32_16x16x32_f16 v[24:27], v[136:139], v[184:187], v[24:27]
	v_mfma_f32_16x16x32_f16 v[12:15], v[128:131], v[192:195], v[12:15]
	v_mfma_f32_16x16x32_f16 v[8:11], v[136:139], v[192:195], v[8:11]
	v_mfma_f32_16x16x32_f16 v[60:63], v[132:135], v[172:175], v[60:63]
	v_mfma_f32_16x16x32_f16 v[56:59], v[140:143], v[172:175], v[56:59]
	v_mfma_f32_16x16x32_f16 v[44:47], v[132:135], v[180:183], v[44:47]
	v_mfma_f32_16x16x32_f16 v[40:43], v[140:143], v[180:183], v[40:43]
	v_mfma_f32_16x16x32_f16 v[28:31], v[132:135], v[188:191], v[28:31]
	v_mfma_f32_16x16x32_f16 v[24:27], v[140:143], v[188:191], v[24:27]
	v_mfma_f32_16x16x32_f16 v[12:15], v[132:135], v[196:199], v[12:15]
	v_mfma_f32_16x16x32_f16 v[8:11], v[140:143], v[196:199], v[8:11]
	s_barrier
	s_add_i32 s34, s34, s40
	s_mov_b32 m0, s34
	v_lshl_add_u64 v[128:129], v[224:225], 0, s[24:25]
	global_load_lds_dwordx4 v[128:129], off
	s_add_i32 m0, s34, 0x2000
	v_lshl_add_u64 v[128:129], v[226:227], 0, s[24:25]
	global_load_lds_dwordx4 v[128:129], off
	s_waitcnt vmcnt(6)
	s_barrier
	v_mfma_f32_16x16x32_f16 v[52:55], v[200:203], v[154:157], v[52:55]
	v_mfma_f32_16x16x32_f16 v[48:51], v[208:211], v[154:157], v[48:51]
	v_mfma_f32_16x16x32_f16 v[36:39], v[200:203], v[176:179], v[36:39]
	v_mfma_f32_16x16x32_f16 v[32:35], v[208:211], v[176:179], v[32:35]
	v_mfma_f32_16x16x32_f16 v[20:23], v[200:203], v[184:187], v[20:23]
	v_mfma_f32_16x16x32_f16 v[16:19], v[208:211], v[184:187], v[16:19]
	v_mfma_f32_16x16x32_f16 v[4:7], v[200:203], v[192:195], v[4:7]
	v_mfma_f32_16x16x32_f16 v[0:3], v[208:211], v[192:195], v[0:3]
	v_mfma_f32_16x16x32_f16 v[52:55], v[204:207], v[172:175], v[52:55]
	v_mfma_f32_16x16x32_f16 v[48:51], v[212:215], v[172:175], v[48:51]
	v_mfma_f32_16x16x32_f16 v[36:39], v[204:207], v[180:183], v[36:39]
	v_mfma_f32_16x16x32_f16 v[32:35], v[212:215], v[180:183], v[32:35]
	v_mfma_f32_16x16x32_f16 v[20:23], v[204:207], v[188:191], v[20:23]
	v_mfma_f32_16x16x32_f16 v[16:19], v[212:215], v[188:191], v[16:19]
	v_mfma_f32_16x16x32_f16 v[4:7], v[204:207], v[196:199], v[4:7]
	v_mfma_f32_16x16x32_f16 v[0:3], v[212:215], v[196:199], v[0:3]
	s_add_u32 s69, s69, 0x100
	s_addc_u32 s70, s70, 0
	s_add_u32 s30, s30, 0x100
	s_addc_u32 s31, s31, 0
	s_cmp_ge_i32 s71, s39
	s_mov_b32 s34, s71
	s_barrier
	s_cbranch_scc0 .LBB3_23
	s_branch .LBB3_10

.LBB3_29:
	s_and_b32 s17, s16, 0x18000
	s_add_i32 s17, s21, s17
	v_lshl_add_u64 v[138:139], v[86:87], 0, s[4:5]
	v_lshl_add_u64 v[90:91], v[138:139], 0, s[6:7]
	s_mov_b32 m0, s17
	v_lshl_add_u64 v[140:141], v[84:85], 0, s[4:5]
	s_waitcnt vmcnt(4)
	s_barrier
	global_load_lds_dwordx4 v[90:91], off
	v_lshl_add_u64 v[90:91], v[140:141], 0, s[6:7]
	s_add_i32 m0, s17, 0x2000
	v_lshl_add_u64 v[142:143], v[82:83], 0, s[4:5]
	global_load_lds_dwordx4 v[90:91], off
	s_add_i32 m0, s17, 0x4000
	v_lshl_add_u64 v[90:91], v[142:143], 0, s[6:7]
	v_lshl_add_u64 v[148:149], v[80:81], 0, s[4:5]
	global_load_lds_dwordx4 v[90:91], off
	s_add_i32 m0, s17, 0x6000
	v_lshl_add_u64 v[90:91], v[148:149], 0, s[6:7]
	global_load_lds_dwordx4 v[90:91], off
	s_waitcnt lgkmcnt(0)
	s_add_i32 s17, s16, 0xfffe8000
	s_and_b32 s17, s17, 0x10000
	v_add_u32_e32 v118, s17, v88
	ds_read_b128 v[90:93], v118 offset:32768
	ds_read_b128 v[94:97], v118 offset:33792
	ds_read_b128 v[98:101], v118 offset:34816
	ds_read_b128 v[102:105], v118 offset:35840
	ds_read_b128 v[106:109], v118 offset:36864
	ds_read_b128 v[110:113], v118 offset:37888
	ds_read_b128 v[114:117], v118 offset:38912
	ds_read_b128 v[118:121], v118 offset:39936
	s_add_i32 s18, s17, 0
	v_add_u32_e32 v134, s18, v161
	ds_read_b128 v[122:125], v134 offset:49152
	ds_read_b128 v[126:129], v134 offset:50176
	ds_read_b128 v[130:133], v134 offset:51200
	ds_read_b128 v[134:137], v134 offset:52224
	v_mfma_f32_16x16x32_f16 v[76:79], v[36:39], v[44:47], v[76:79]
	v_mfma_f32_16x16x32_f16 v[44:47], v[28:31], v[44:47], v[72:75]
	v_mfma_f32_16x16x32_f16 v[76:79], v[32:35], v[40:43], v[76:79]
	v_mfma_f32_16x16x32_f16 v[72:75], v[24:27], v[40:43], v[44:47]
	v_mfma_f32_16x16x32_f16 v[40:43], v[36:39], v[20:23], v[68:71]
	v_mfma_f32_16x16x32_f16 v[20:23], v[28:31], v[20:23], v[64:67]
	v_mfma_f32_16x16x32_f16 v[68:71], v[32:35], v[16:19], v[40:43]
	v_mfma_f32_16x16x32_f16 v[64:67], v[24:27], v[16:19], v[20:23]
	v_mfma_f32_16x16x32_f16 v[16:19], v[36:39], v[12:15], v[60:63]
	v_mfma_f32_16x16x32_f16 v[12:15], v[28:31], v[12:15], v[56:59]
	v_mfma_f32_16x16x32_f16 v[60:63], v[32:35], v[8:11], v[16:19]
	v_mfma_f32_16x16x32_f16 v[56:59], v[24:27], v[8:11], v[12:15]
	v_mfma_f32_16x16x32_f16 v[8:11], v[36:39], v[4:7], v[52:55]
	v_mfma_f32_16x16x32_f16 v[4:7], v[28:31], v[4:7], v[48:51]
	v_mfma_f32_16x16x32_f16 v[52:55], v[32:35], v[0:3], v[8:11]
	v_mfma_f32_16x16x32_f16 v[48:51], v[24:27], v[0:3], v[4:7]
	s_add_i32 s19, s21, s17
	v_lshl_add_u64 v[0:1], v[138:139], 0, s[14:15]
	s_mov_b32 m0, s19
	s_waitcnt vmcnt(4)
	s_barrier
	global_load_lds_dwordx4 v[0:1], off
	v_lshl_add_u64 v[0:1], v[140:141], 0, s[14:15]
	s_add_i32 m0, s19, 0x2000
	s_add_i32 s18, s18, s40
	global_load_lds_dwordx4 v[0:1], off
	s_add_i32 m0, s18, 0x4000
	v_lshl_add_u64 v[0:1], v[142:143], 0, s[14:15]
	global_load_lds_dwordx4 v[0:1], off
	s_add_i32 m0, s18, 0x6000
	v_lshl_add_u64 v[0:1], v[148:149], 0, s[14:15]
	global_load_lds_dwordx4 v[0:1], off
	s_waitcnt lgkmcnt(0)
	s_xor_b32 s17, s17, 0x10000
	v_add_u32_e32 v0, s17, v88
	ds_read_b128 v[44:47], v0
	ds_read_b128 v[40:43], v0 offset:1024
	ds_read_b128 v[20:23], v0 offset:2048
	ds_read_b128 v[16:19], v0 offset:3072
	ds_read_b128 v[12:15], v0 offset:4096
	ds_read_b128 v[8:11], v0 offset:5120
	ds_read_b128 v[4:7], v0 offset:6144
	ds_read_b128 v[0:3], v0 offset:7168
	v_add_u32_e32 v24, s17, v89
	ds_read_b128 v[36:39], v24 offset:16384
	ds_read_b128 v[32:35], v24 offset:17408
	ds_read_b128 v[28:31], v24 offset:18432
	ds_read_b128 v[24:27], v24 offset:19456
	v_mfma_f32_16x16x32_f16 v[76:79], v[122:125], v[90:93], v[76:79]
	v_mfma_f32_16x16x32_f16 v[72:75], v[130:133], v[90:93], v[72:75]
	v_mfma_f32_16x16x32_f16 v[68:71], v[122:125], v[98:101], v[68:71]
	v_mfma_f32_16x16x32_f16 v[64:67], v[130:133], v[98:101], v[64:67]
	v_mfma_f32_16x16x32_f16 v[60:63], v[122:125], v[106:109], v[60:63]
	v_mfma_f32_16x16x32_f16 v[56:59], v[130:133], v[106:109], v[56:59]
	v_mfma_f32_16x16x32_f16 v[52:55], v[122:125], v[114:117], v[52:55]
	v_mfma_f32_16x16x32_f16 v[48:51], v[130:133], v[114:117], v[48:51]
	v_mfma_f32_16x16x32_f16 v[76:79], v[126:129], v[94:97], v[76:79]
	v_mfma_f32_16x16x32_f16 v[72:75], v[134:137], v[94:97], v[72:75]
	v_mfma_f32_16x16x32_f16 v[68:71], v[126:129], v[102:105], v[68:71]
	v_mfma_f32_16x16x32_f16 v[64:67], v[134:137], v[102:105], v[64:67]
	v_mfma_f32_16x16x32_f16 v[60:63], v[126:129], v[110:113], v[60:63]
	v_mfma_f32_16x16x32_f16 v[56:59], v[134:137], v[110:113], v[56:59]
	v_mfma_f32_16x16x32_f16 v[52:55], v[126:129], v[118:121], v[52:55]
	v_mfma_f32_16x16x32_f16 v[48:51], v[134:137], v[118:121], v[48:51]
	s_add_i32 s22, s22, 2
	s_add_i32 s16, s16, 0x10000
	s_add_u32 s4, s4, 0x100
	s_addc_u32 s5, s5, 0
	s_cmp_ge_i32 s22, s23
	s_cbranch_scc0 .LBB3_29
	s_branch .LBB3_31

.LBB3_31:
	s_add_i32 s4, s39, -1
	s_ashr_i32 s5, s4, 31
	s_lshl_b64 s[6:7], s[4:5], 7
	s_add_u32 s0, s0, s6
	s_addc_u32 s1, s1, s7
	s_lshl_b32 s4, s4, 15
	s_and_b32 s4, s4, 0x18000
	s_add_i32 s4, s4, 0
	s_add_i32 s4, s4, s40
	v_lshl_add_u64 v[80:81], s[0:1], 0, v[144:145]
	s_mov_b32 m0, s4
	s_waitcnt vmcnt(4)
	s_barrier
	global_load_lds_dwordx4 v[80:81], off
	s_add_i32 m0, s4, 0x2000
	v_lshl_add_u64 v[80:81], s[0:1], 0, v[146:147]
	s_add_u32 s0, s2, s6
	s_addc_u32 s1, s3, s7
	global_load_lds_dwordx4 v[80:81], off
	s_add_i32 m0, s4, 0x4000
	v_lshl_add_u64 v[80:81], s[0:1], 0, v[144:145]
	global_load_lds_dwordx4 v[80:81], off
	s_add_i32 m0, s4, 0x6000
	v_lshl_add_u64 v[80:81], s[0:1], 0, v[146:147]
	global_load_lds_dwordx4 v[80:81], off
	s_waitcnt lgkmcnt(0)
	s_lshl_b32 s0, s39, 15
	s_add_i32 s1, s0, 0x8000
	s_and_b32 s1, s1, 0x18000
	s_add_i32 s1, s1, 0
	v_add_u32_e32 v108, s1, v160
	ds_read_b128 v[80:83], v108
	ds_read_b128 v[84:87], v108 offset:1024
	ds_read_b128 v[88:91], v108 offset:2048
	ds_read_b128 v[92:95], v108 offset:3072
	ds_read_b128 v[96:99], v108 offset:4096
	ds_read_b128 v[100:103], v108 offset:5120
	ds_read_b128 v[104:107], v108 offset:6144
	ds_read_b128 v[108:111], v108 offset:7168
	v_add_u32_e32 v124, s1, v161
	ds_read_b128 v[112:115], v124 offset:16384
	ds_read_b128 v[116:119], v124 offset:17408
	ds_read_b128 v[120:123], v124 offset:18432
	ds_read_b128 v[124:127], v124 offset:19456
	v_mfma_f32_16x16x32_f16 v[76:79], v[36:39], v[44:47], v[76:79]
	v_mfma_f32_16x16x32_f16 v[44:47], v[28:31], v[44:47], v[72:75]
	v_mfma_f32_16x16x32_f16 v[76:79], v[32:35], v[40:43], v[76:79]
	v_mfma_f32_16x16x32_f16 v[40:43], v[24:27], v[40:43], v[44:47]
	v_mfma_f32_16x16x32_f16 v[44:47], v[36:39], v[20:23], v[68:71]
	v_mfma_f32_16x16x32_f16 v[20:23], v[28:31], v[20:23], v[64:67]
	v_mfma_f32_16x16x32_f16 v[44:47], v[32:35], v[16:19], v[44:47]
	v_mfma_f32_16x16x32_f16 v[16:19], v[24:27], v[16:19], v[20:23]
	v_mfma_f32_16x16x32_f16 v[20:23], v[36:39], v[12:15], v[60:63]
	v_mfma_f32_16x16x32_f16 v[12:15], v[28:31], v[12:15], v[56:59]
	v_mfma_f32_16x16x32_f16 v[20:23], v[32:35], v[8:11], v[20:23]
	v_mfma_f32_16x16x32_f16 v[8:11], v[24:27], v[8:11], v[12:15]
	v_mfma_f32_16x16x32_f16 v[12:15], v[36:39], v[4:7], v[52:55]
	v_mfma_f32_16x16x32_f16 v[4:7], v[28:31], v[4:7], v[48:51]
	v_mfma_f32_16x16x32_f16 v[12:15], v[32:35], v[0:3], v[12:15]
	v_mfma_f32_16x16x32_f16 v[0:3], v[24:27], v[0:3], v[4:7]
	s_waitcnt vmcnt(4)
	s_barrier
	s_waitcnt lgkmcnt(0)
	s_and_b32 s1, s0, 0x18000
	s_xor_b32 s1, s1, 0x10000
	s_add_i32 s1, s1, 0
	v_add_u32_e32 v56, s1, v160
	ds_read_b128 v[4:7], v56
	ds_read_b128 v[24:27], v56 offset:1024
	ds_read_b128 v[28:31], v56 offset:2048
	ds_read_b128 v[32:35], v56 offset:3072
	ds_read_b128 v[36:39], v56 offset:4096
	ds_read_b128 v[48:51], v56 offset:5120
	ds_read_b128 v[52:55], v56 offset:6144
	ds_read_b128 v[56:59], v56 offset:7168
	v_add_u32_e32 v72, s1, v161
	ds_read_b128 v[60:63], v72 offset:16384
	ds_read_b128 v[64:67], v72 offset:17408
	ds_read_b128 v[68:71], v72 offset:18432
	ds_read_b128 v[72:75], v72 offset:19456
	v_mfma_f32_16x16x32_f16 v[76:79], v[112:115], v[80:83], v[76:79]
	v_mfma_f32_16x16x32_f16 v[40:43], v[120:123], v[80:83], v[40:43]
	v_mfma_f32_16x16x32_f16 v[44:47], v[112:115], v[88:91], v[44:47]
	v_mfma_f32_16x16x32_f16 v[16:19], v[120:123], v[88:91], v[16:19]
	v_mfma_f32_16x16x32_f16 v[20:23], v[112:115], v[96:99], v[20:23]
	v_mfma_f32_16x16x32_f16 v[8:11], v[120:123], v[96:99], v[8:11]
	v_mfma_f32_16x16x32_f16 v[12:15], v[112:115], v[104:107], v[12:15]
	v_mfma_f32_16x16x32_f16 v[0:3], v[120:123], v[104:107], v[0:3]
	v_mfma_f32_16x16x32_f16 v[76:79], v[116:119], v[84:87], v[76:79]
	v_mfma_f32_16x16x32_f16 v[40:43], v[124:127], v[84:87], v[40:43]
	v_mfma_f32_16x16x32_f16 v[44:47], v[116:119], v[92:95], v[44:47]
	v_mfma_f32_16x16x32_f16 v[16:19], v[124:127], v[92:95], v[16:19]
	v_mfma_f32_16x16x32_f16 v[20:23], v[116:119], v[100:103], v[20:23]
	v_mfma_f32_16x16x32_f16 v[8:11], v[124:127], v[100:103], v[8:11]
	v_mfma_f32_16x16x32_f16 v[12:15], v[116:119], v[108:111], v[12:15]
	v_mfma_f32_16x16x32_f16 v[0:3], v[124:127], v[108:111], v[0:3]
	s_waitcnt vmcnt(0)
	s_barrier
	s_waitcnt lgkmcnt(0)
	s_add_i32 s0, s0, 0x18000
	s_and_b32 s0, s0, 0x18000
	s_add_i32 s0, s0, 0
	v_add_u32_e32 v108, s0, v160
	ds_read_b128 v[80:83], v108
	ds_read_b128 v[84:87], v108 offset:1024
	ds_read_b128 v[88:91], v108 offset:2048
	ds_read_b128 v[92:95], v108 offset:3072
	ds_read_b128 v[96:99], v108 offset:4096
	ds_read_b128 v[100:103], v108 offset:5120
	ds_read_b128 v[104:107], v108 offset:6144
	ds_read_b128 v[108:111], v108 offset:7168
	v_add_u32_e32 v124, s0, v161
	ds_read_b128 v[112:115], v124 offset:16384
	ds_read_b128 v[116:119], v124 offset:17408
	ds_read_b128 v[120:123], v124 offset:18432
	ds_read_b128 v[124:127], v124 offset:19456
	v_mfma_f32_16x16x32_f16 v[76:79], v[60:63], v[4:7], v[76:79]
	v_mfma_f32_16x16x32_f16 v[4:7], v[68:71], v[4:7], v[40:43]
	v_mfma_f32_16x16x32_f16 v[76:79], v[64:67], v[24:27], v[76:79]
	v_mfma_f32_16x16x32_f16 v[4:7], v[72:75], v[24:27], v[4:7]
	v_mfma_f32_16x16x32_f16 v[24:27], v[60:63], v[28:31], v[44:47]
	v_mfma_f32_16x16x32_f16 v[16:19], v[68:71], v[28:31], v[16:19]
	v_mfma_f32_16x16x32_f16 v[20:23], v[60:63], v[36:39], v[20:23]
	v_mfma_f32_16x16x32_f16 v[8:11], v[68:71], v[36:39], v[8:11]
	v_mfma_f32_16x16x32_f16 v[12:15], v[60:63], v[52:55], v[12:15]
	v_mfma_f32_16x16x32_f16 v[0:3], v[68:71], v[52:55], v[0:3]
	v_mfma_f32_16x16x32_f16 v[24:27], v[64:67], v[32:35], v[24:27]
	v_mfma_f32_16x16x32_f16 v[16:19], v[72:75], v[32:35], v[16:19]
	v_mfma_f32_16x16x32_f16 v[20:23], v[64:67], v[48:51], v[20:23]
	v_mfma_f32_16x16x32_f16 v[8:11], v[72:75], v[48:51], v[8:11]
	v_mfma_f32_16x16x32_f16 v[12:15], v[64:67], v[56:59], v[12:15]
	v_mfma_f32_16x16x32_f16 v[0:3], v[72:75], v[56:59], v[0:3]
	v_lshl_or_b32 v32, v159, 2, s38
	v_or_b32_e32 v32, s20, v32
	v_ashrrev_i32_e32 v33, 31, v32
	v_lshlrev_b64 v[40:41], 2, v[32:33]
	v_lshl_add_u64 v[36:37], s[10:11], 0, v[40:41]
	global_load_dwordx4 v[32:35], v[36:37], off
	s_waitcnt lgkmcnt(0)
	v_mfma_f32_16x16x32_f16 v[28:31], v[112:115], v[80:83], v[76:79]
	global_load_dwordx4 v[36:39], v[36:37], off offset:64
	s_add_i32 s33, s33, s12
	v_or_b32_e32 v44, s33, v158
	v_mfma_f32_16x16x32_f16 v[4:7], v[120:123], v[80:83], v[4:7]
	v_mad_i64_i32 v[42:43], s[0:1], v44, s13, 0
	v_or_b32_e32 v45, 16, v44
	v_mfma_f32_16x16x32_f16 v[24:27], v[112:115], v[88:91], v[24:27]
	v_or_b32_e32 v46, 32, v44
	v_or_b32_e32 v48, 48, v44
	v_lshl_add_u64 v[40:41], s[8:9], 0, v[40:41]
	v_mfma_f32_16x16x32_f16 v[16:19], v[120:123], v[88:91], v[16:19]
	v_mad_i64_i32 v[44:45], s[0:1], v45, s13, 0
	v_mad_i64_i32 v[46:47], s[0:1], v46, s13, 0
	v_mfma_f32_16x16x32_f16 v[20:23], v[112:115], v[96:99], v[20:23]
	v_mad_i64_i32 v[48:49], s[0:1], v48, s13, 0
	v_lshl_add_u64 v[42:43], v[42:43], 2, v[40:41]
	v_mfma_f32_16x16x32_f16 v[8:11], v[120:123], v[96:99], v[8:11]
	v_lshl_add_u64 v[44:45], v[44:45], 2, v[40:41]
	v_lshl_add_u64 v[46:47], v[46:47], 2, v[40:41]
	v_lshl_add_u64 v[40:41], v[48:49], 2, v[40:41]
	v_mfma_f32_16x16x32_f16 v[12:15], v[112:115], v[104:107], v[12:15]
	v_mfma_f32_16x16x32_f16 v[0:3], v[120:123], v[104:107], v[0:3]
	v_mfma_f32_16x16x32_f16 v[28:31], v[116:119], v[84:87], v[28:31]
	v_mfma_f32_16x16x32_f16 v[4:7], v[124:127], v[84:87], v[4:7]
	v_mfma_f32_16x16x32_f16 v[24:27], v[116:119], v[92:95], v[24:27]
	s_waitcnt vmcnt(0)
	s_nop 4
	v_pk_add_f32 v[30:31], v[34:35], v[30:31]
	v_mfma_f32_16x16x32_f16 v[16:19], v[124:127], v[92:95], v[16:19]
	v_add_f32_e64 v28, v32, v28
	v_add_f32_e64 v29, v33, v29
	v_pk_add_f32 v[6:7], v[38:39], v[6:7]
	v_pk_add_f32 v[4:5], v[36:37], v[4:5]
	v_mfma_f32_16x16x32_f16 v[20:23], v[116:119], v[100:103], v[20:23]
	v_add_f32_e64 v26, v34, v26
	v_add_f32_e64 v27, v35, v27
	v_pk_add_f32 v[24:25], v[32:33], v[24:25]
	v_pk_add_f32 v[18:19], v[38:39], v[18:19]
	v_mfma_f32_16x16x32_f16 v[8:11], v[124:127], v[100:103], v[8:11]
	v_add_f32_e64 v16, v36, v16
	v_add_f32_e64 v17, v37, v17
	s_nop 0
	v_pk_add_f32 v[22:23], v[34:35], v[22:23]
	v_pk_add_f32 v[20:21], v[32:33], v[20:21]
	v_mfma_f32_16x16x32_f16 v[12:15], v[116:119], v[108:111], v[12:15]
	v_mfma_f32_16x16x32_f16 v[0:3], v[124:127], v[108:111], v[0:3]
	s_nop 0
	v_add_f32_e64 v10, v38, v10
	v_add_f32_e64 v11, v39, v11
	v_pk_add_f32 v[8:9], v[36:37], v[8:9]
	s_nop 2
	v_pk_add_f32 v[14:15], v[34:35], v[14:15]
	v_pk_add_f32 v[12:13], v[32:33], v[12:13]
	v_pk_add_f32 v[2:3], v[38:39], v[2:3]
	v_pk_add_f32 v[0:1], v[36:37], v[0:1]
	global_store_dwordx4 v[42:43], v[28:31], off
	global_store_dwordx4 v[42:43], v[4:7], off offset:64
	global_store_dwordx4 v[44:45], v[24:27], off
	global_store_dwordx4 v[44:45], v[16:19], off offset:64
	global_store_dwordx4 v[46:47], v[20:23], off
	global_store_dwordx4 v[46:47], v[8:11], off offset:64
	global_store_dwordx4 v[40:41], v[12:15], off
	global_store_dwordx4 v[40:41], v[0:3], off offset:64
	s_bitcmp1_b32 s82, 5
	s_cbranch_scc0 .Lg1_done
	s_cmp_eq_u32 s84, 0
	s_cbranch_scc0 .Lg1_done
	s_mov_b32 s84, 1
	s_waitcnt lgkmcnt(0)
	s_barrier
	s_mov_b64 exec, -1
	s_mov_b64 s[0:1], s[80:81]
	s_mov_b32 s2, s82
	v_mbcnt_lo_u32_b32 v0, -1, 0
	v_mbcnt_hi_u32_b32 v0, -1, v0
	v_add_u32_e32 v0, s83, v0
	s_branch .Lg1_restart
